# both gemm1 K-loops: first MFMAs of a tile issued ahead of the per-tile barrier so the matrix pipe runs through the barrier wait
# speedup vs baseline: 1.0066x; 1.0066x over previous
.LBB1_2:
	s_waitcnt lgkmcnt(0)
	v_mfma_f32_16x16x32_f16 v[14:17], v[62:65], v[58:61], v[14:17]
	v_mfma_f32_16x16x32_f16 v[30:33], v[54:57], v[58:61], v[30:33]
	v_mfma_f32_16x16x32_f16 v[22:25], v[54:57], v[66:69], v[22:25]
	s_waitcnt vmcnt(9)
	s_barrier
	s_lshl_b32 s28, s38, 15
	v_or_b32_e32 v53, s28, v50
	v_add_u32_e32 v88, s28, v92
	v_add_u32_e32 v53, v53, v52
	v_add_u32_e32 v89, s28, v93
	v_cndmask_b32_e64 v88, v88, v95, s[42:43]
	v_add_u32_e32 v95, 64, v95
	s_lshl_b32 s29, s37, 15
	s_add_u32 s30, s29, s41
	s_add_u32 s31, s29, s40
	ds_read_b128 v[100:103], v53
	ds_read_b128 v[104:107], v88 offset:16384
	v_mfma_f32_16x16x32_f16 v[6:9], v[62:65], v[66:69], v[6:9]
	ds_read_b128 v[108:111], v53 offset:1024
	v_mfma_f32_16x16x32_f16 v[26:29], v[54:57], v[70:73], v[26:29]
	ds_read_b128 v[112:115], v89 offset:16384
	v_mfma_f32_16x16x32_f16 v[30:33], v[80:83], v[58:61], v[30:33]
	ds_read_b128 v[116:119], v88 offset:18432
	v_mfma_f32_16x16x32_f16 v[22:25], v[80:83], v[66:69], v[22:25]
	ds_read_b128 v[120:123], v89 offset:18432
	v_mfma_f32_16x16x32_f16 v[18:21], v[54:57], v[74:77], v[18:21]
	ds_read_b128 v[124:127], v53 offset:8192
	v_mfma_f32_16x16x32_f16 v[14:17], v[84:87], v[58:61], v[14:17]
	ds_read_b128 v[128:131], v53 offset:9216
	s_mov_b32 m0, s30
	v_lshl_add_u64 v[96:97], v[40:41], 0, s[26:27]
	global_load_lds_dwordx4 v[96:97], off
	v_mfma_f32_16x16x32_f16 v[10:13], v[62:65], v[70:73], v[10:13]
	s_add_u32 m0, s30, 0x2000
	v_lshl_add_u64 v[96:97], v[38:39], 0, s[26:27]
	global_load_lds_dwordx4 v[96:97], off
	v_mfma_f32_16x16x32_f16 v[6:9], v[84:87], v[66:69], v[6:9]
	s_mov_b32 m0, s31
	v_lshl_add_u64 v[96:97], v[36:37], 0, s[26:27]
	global_load_lds_dwordx4 v[96:97], off
	v_mfma_f32_16x16x32_f16 v[2:5], v[62:65], v[74:77], v[2:5]
	s_add_i32 s36, s36, 1
	s_add_u32 s26, s26, 64
	s_add_i32 s28, s37, 1
	s_cmp_lg_u32 s37, 4
	s_cselect_b32 s37, s28, 0
	s_add_i32 s28, s38, 1
	s_cmp_lg_u32 s38, 4
	s_cselect_b32 s38, s28, 0
	s_waitcnt lgkmcnt(0)
	v_mfma_f32_16x16x32_f16 v[14:17], v[108:111], v[104:107], v[14:17]
	v_mfma_f32_16x16x32_f16 v[30:33], v[100:103], v[104:107], v[30:33]
	v_mfma_f32_16x16x32_f16 v[22:25], v[100:103], v[112:115], v[22:25]
	s_waitcnt vmcnt(9)
	s_barrier
	s_lshl_b32 s28, s38, 15
	v_or_b32_e32 v53, s28, v50
	v_add_u32_e32 v88, s28, v92
	v_add_u32_e32 v53, v53, v52
	v_add_u32_e32 v89, s28, v93
	v_cndmask_b32_e64 v88, v88, v95, s[42:43]
	v_add_u32_e32 v95, 64, v95
	s_lshl_b32 s29, s37, 15
	s_add_u32 s30, s29, s41
	s_add_u32 s31, s29, s40
	ds_read_b128 v[54:57], v53
	ds_read_b128 v[58:61], v88 offset:16384
	v_mfma_f32_16x16x32_f16 v[6:9], v[108:111], v[112:115], v[6:9]
	ds_read_b128 v[62:65], v53 offset:1024
	v_mfma_f32_16x16x32_f16 v[26:29], v[100:103], v[116:119], v[26:29]
	ds_read_b128 v[66:69], v89 offset:16384
	v_mfma_f32_16x16x32_f16 v[30:33], v[124:127], v[104:107], v[30:33]
	ds_read_b128 v[70:73], v88 offset:18432
	v_mfma_f32_16x16x32_f16 v[22:25], v[124:127], v[112:115], v[22:25]
	ds_read_b128 v[74:77], v89 offset:18432
	v_mfma_f32_16x16x32_f16 v[18:21], v[100:103], v[120:123], v[18:21]
	ds_read_b128 v[80:83], v53 offset:8192
	v_mfma_f32_16x16x32_f16 v[14:17], v[128:131], v[104:107], v[14:17]
	ds_read_b128 v[84:87], v53 offset:9216
	s_mov_b32 m0, s30
	v_lshl_add_u64 v[96:97], v[40:41], 0, s[26:27]
	global_load_lds_dwordx4 v[96:97], off
	v_mfma_f32_16x16x32_f16 v[10:13], v[108:111], v[116:119], v[10:13]
	s_add_u32 m0, s30, 0x2000
	v_lshl_add_u64 v[96:97], v[38:39], 0, s[26:27]
	global_load_lds_dwordx4 v[96:97], off
	v_mfma_f32_16x16x32_f16 v[6:9], v[128:131], v[112:115], v[6:9]
	s_mov_b32 m0, s31
	v_lshl_add_u64 v[96:97], v[36:37], 0, s[26:27]
	global_load_lds_dwordx4 v[96:97], off
	v_mfma_f32_16x16x32_f16 v[2:5], v[108:111], v[120:123], v[2:5]
	s_add_i32 s36, s36, 1
	s_add_u32 s26, s26, 64
	s_add_i32 s28, s37, 1
	s_cmp_lg_u32 s37, 4
	s_cselect_b32 s37, s28, 0
	s_add_i32 s28, s38, 1
	s_cmp_lg_u32 s38, 4
	s_cselect_b32 s38, s28, 0
	s_cmp_lt_u32 s36, 26
	s_cbranch_scc1 .LBB1_2
	s_waitcnt lgkmcnt(0)
	v_mfma_f32_16x16x32_f16 v[14:17], v[62:65], v[58:61], v[14:17]
	v_mfma_f32_16x16x32_f16 v[30:33], v[54:57], v[58:61], v[30:33]
	v_mfma_f32_16x16x32_f16 v[22:25], v[54:57], v[66:69], v[22:25]
	s_waitcnt vmcnt(9)
	s_barrier
	s_lshl_b32 s28, s38, 15
	v_or_b32_e32 v53, s28, v50
	v_add_u32_e32 v88, s28, v92
	v_add_u32_e32 v53, v53, v52
	v_add_u32_e32 v89, s28, v93
	v_cndmask_b32_e64 v88, v88, v95, s[42:43]
	v_add_u32_e32 v95, 64, v95
	s_lshl_b32 s29, s37, 15
	s_add_u32 s30, s29, s41
	s_add_u32 s31, s29, s40
	ds_read_b128 v[100:103], v53
	ds_read_b128 v[104:107], v88 offset:16384
	v_mfma_f32_16x16x32_f16 v[6:9], v[62:65], v[66:69], v[6:9]
	ds_read_b128 v[108:111], v53 offset:1024
	v_mfma_f32_16x16x32_f16 v[26:29], v[54:57], v[70:73], v[26:29]
	ds_read_b128 v[112:115], v89 offset:16384
	v_mfma_f32_16x16x32_f16 v[30:33], v[80:83], v[58:61], v[30:33]
	ds_read_b128 v[116:119], v88 offset:18432
	v_mfma_f32_16x16x32_f16 v[22:25], v[80:83], v[66:69], v[22:25]
	ds_read_b128 v[120:123], v89 offset:18432
	v_mfma_f32_16x16x32_f16 v[18:21], v[54:57], v[74:77], v[18:21]
	ds_read_b128 v[124:127], v53 offset:8192
	v_mfma_f32_16x16x32_f16 v[14:17], v[84:87], v[58:61], v[14:17]
	ds_read_b128 v[128:131], v53 offset:9216
	s_mov_b32 m0, s30
	v_lshl_add_u64 v[96:97], v[40:41], 0, s[26:27]
	global_load_lds_dwordx4 v[96:97], off
	v_mfma_f32_16x16x32_f16 v[10:13], v[62:65], v[70:73], v[10:13]
	s_add_u32 m0, s30, 0x2000
	v_lshl_add_u64 v[96:97], v[38:39], 0, s[26:27]
	global_load_lds_dwordx4 v[96:97], off
	v_mfma_f32_16x16x32_f16 v[6:9], v[84:87], v[66:69], v[6:9]
	s_mov_b32 m0, s31
	v_lshl_add_u64 v[96:97], v[36:37], 0, s[26:27]
	global_load_lds_dwordx4 v[96:97], off
	v_mfma_f32_16x16x32_f16 v[2:5], v[62:65], v[74:77], v[2:5]
	s_add_i32 s36, s36, 1
	s_add_u32 s26, s26, 64
	s_add_i32 s28, s37, 1
	s_cmp_lg_u32 s37, 4
	s_cselect_b32 s37, s28, 0
	s_add_i32 s28, s38, 1
	s_cmp_lg_u32 s38, 4
	s_cselect_b32 s38, s28, 0
	s_waitcnt lgkmcnt(0)
	v_mfma_f32_16x16x32_f16 v[14:17], v[108:111], v[104:107], v[14:17]
	v_mfma_f32_16x16x32_f16 v[30:33], v[100:103], v[104:107], v[30:33]
	v_mfma_f32_16x16x32_f16 v[22:25], v[100:103], v[112:115], v[22:25]
	s_waitcnt vmcnt(9)
	s_barrier
	s_lshl_b32 s28, s38, 15
	v_or_b32_e32 v53, s28, v50
	v_add_u32_e32 v88, s28, v92
	v_add_u32_e32 v53, v53, v52
	v_add_u32_e32 v89, s28, v93
	v_cndmask_b32_e64 v88, v88, v95, s[42:43]
	v_add_u32_e32 v95, 64, v95
	ds_read_b128 v[54:57], v53
	ds_read_b128 v[58:61], v88 offset:16384
	v_mfma_f32_16x16x32_f16 v[6:9], v[108:111], v[112:115], v[6:9]
	ds_read_b128 v[62:65], v53 offset:1024
	v_mfma_f32_16x16x32_f16 v[26:29], v[100:103], v[116:119], v[26:29]
	ds_read_b128 v[66:69], v89 offset:16384
	v_mfma_f32_16x16x32_f16 v[30:33], v[124:127], v[104:107], v[30:33]
	ds_read_b128 v[70:73], v88 offset:18432
	v_mfma_f32_16x16x32_f16 v[22:25], v[124:127], v[112:115], v[22:25]
	ds_read_b128 v[74:77], v89 offset:18432
	v_mfma_f32_16x16x32_f16 v[18:21], v[100:103], v[120:123], v[18:21]
	ds_read_b128 v[80:83], v53 offset:8192
	v_mfma_f32_16x16x32_f16 v[14:17], v[128:131], v[104:107], v[14:17]
	ds_read_b128 v[84:87], v53 offset:9216
	v_mfma_f32_16x16x32_f16 v[10:13], v[108:111], v[116:119], v[10:13]
	v_mfma_f32_16x16x32_f16 v[6:9], v[128:131], v[112:115], v[6:9]
	v_mfma_f32_16x16x32_f16 v[2:5], v[108:111], v[120:123], v[2:5]
	s_add_i32 s36, s36, 1
	s_add_u32 s26, s26, 64
	s_add_i32 s28, s37, 1
	s_cmp_lg_u32 s37, 4
	s_cselect_b32 s37, s28, 0
	s_add_i32 s28, s38, 1
	s_cmp_lg_u32 s38, 4
	s_cselect_b32 s38, s28, 0
	s_waitcnt lgkmcnt(0)
	v_mfma_f32_16x16x32_f16 v[14:17], v[62:65], v[58:61], v[14:17]
	v_mfma_f32_16x16x32_f16 v[30:33], v[54:57], v[58:61], v[30:33]
	v_mfma_f32_16x16x32_f16 v[22:25], v[54:57], v[66:69], v[22:25]
	s_waitcnt vmcnt(6)
	s_barrier
	s_lshl_b32 s28, s38, 15
	v_or_b32_e32 v53, s28, v50
	v_add_u32_e32 v88, s28, v92
	v_add_u32_e32 v53, v53, v52
	v_add_u32_e32 v89, s28, v93
	v_cndmask_b32_e64 v88, v88, v95, s[42:43]
	v_add_u32_e32 v95, 64, v95
	ds_read_b128 v[100:103], v53
	ds_read_b128 v[104:107], v88 offset:16384
	v_mfma_f32_16x16x32_f16 v[6:9], v[62:65], v[66:69], v[6:9]
	ds_read_b128 v[108:111], v53 offset:1024
	v_mfma_f32_16x16x32_f16 v[26:29], v[54:57], v[70:73], v[26:29]
	ds_read_b128 v[112:115], v89 offset:16384
	v_mfma_f32_16x16x32_f16 v[30:33], v[80:83], v[58:61], v[30:33]
	ds_read_b128 v[116:119], v88 offset:18432
	v_mfma_f32_16x16x32_f16 v[22:25], v[80:83], v[66:69], v[22:25]
	ds_read_b128 v[120:123], v89 offset:18432
	v_mfma_f32_16x16x32_f16 v[18:21], v[54:57], v[74:77], v[18:21]
	ds_read_b128 v[124:127], v53 offset:8192
	v_mfma_f32_16x16x32_f16 v[14:17], v[84:87], v[58:61], v[14:17]
	ds_read_b128 v[128:131], v53 offset:9216
	v_mfma_f32_16x16x32_f16 v[10:13], v[62:65], v[70:73], v[10:13]
	v_mfma_f32_16x16x32_f16 v[6:9], v[84:87], v[66:69], v[6:9]
	v_mfma_f32_16x16x32_f16 v[2:5], v[62:65], v[74:77], v[2:5]
	s_add_i32 s36, s36, 1
	s_add_u32 s26, s26, 64
	s_add_i32 s28, s37, 1
	s_cmp_lg_u32 s37, 4
	s_cselect_b32 s37, s28, 0
	s_add_i32 s28, s38, 1
	s_cmp_lg_u32 s38, 4
	s_cselect_b32 s38, s28, 0
	s_waitcnt lgkmcnt(0)
	v_mfma_f32_16x16x32_f16 v[14:17], v[108:111], v[104:107], v[14:17]
	v_mfma_f32_16x16x32_f16 v[30:33], v[100:103], v[104:107], v[30:33]
	v_mfma_f32_16x16x32_f16 v[22:25], v[100:103], v[112:115], v[22:25]
	s_waitcnt vmcnt(3)
	s_barrier
	s_lshl_b32 s28, s38, 15
	v_or_b32_e32 v53, s28, v50
	v_add_u32_e32 v88, s28, v92
	v_add_u32_e32 v53, v53, v52
	v_add_u32_e32 v89, s28, v93
	v_cndmask_b32_e64 v88, v88, v95, s[42:43]
	v_add_u32_e32 v95, 64, v95
	ds_read_b128 v[54:57], v53
	ds_read_b128 v[58:61], v88 offset:16384
	v_mfma_f32_16x16x32_f16 v[6:9], v[108:111], v[112:115], v[6:9]
	ds_read_b128 v[62:65], v53 offset:1024
	v_mfma_f32_16x16x32_f16 v[26:29], v[100:103], v[116:119], v[26:29]
	ds_read_b128 v[66:69], v89 offset:16384
	v_mfma_f32_16x16x32_f16 v[30:33], v[124:127], v[104:107], v[30:33]
	ds_read_b128 v[70:73], v88 offset:18432
	v_mfma_f32_16x16x32_f16 v[22:25], v[124:127], v[112:115], v[22:25]
	ds_read_b128 v[74:77], v89 offset:18432
	v_mfma_f32_16x16x32_f16 v[18:21], v[100:103], v[120:123], v[18:21]
	ds_read_b128 v[80:83], v53 offset:8192
	v_mfma_f32_16x16x32_f16 v[14:17], v[128:131], v[104:107], v[14:17]
	ds_read_b128 v[84:87], v53 offset:9216
	v_mfma_f32_16x16x32_f16 v[10:13], v[108:111], v[116:119], v[10:13]
	v_mfma_f32_16x16x32_f16 v[6:9], v[128:131], v[112:115], v[6:9]
	v_mfma_f32_16x16x32_f16 v[2:5], v[108:111], v[120:123], v[2:5]
	s_add_i32 s36, s36, 1
	s_add_u32 s26, s26, 64
	s_add_i32 s28, s37, 1
	s_cmp_lg_u32 s37, 4
	s_cselect_b32 s37, s28, 0
	s_add_i32 s28, s38, 1
	s_cmp_lg_u32 s38, 4
	s_cselect_b32 s38, s28, 0
	s_waitcnt lgkmcnt(0)
	v_mfma_f32_16x16x32_f16 v[14:17], v[62:65], v[58:61], v[14:17]
	v_mfma_f32_16x16x32_f16 v[30:33], v[54:57], v[58:61], v[30:33]
	v_mfma_f32_16x16x32_f16 v[22:25], v[54:57], v[66:69], v[22:25]
	s_waitcnt vmcnt(0)
	s_barrier
	s_lshl_b32 s28, s38, 15
	v_or_b32_e32 v53, s28, v50
	v_add_u32_e32 v88, s28, v92
	v_add_u32_e32 v53, v53, v52
	v_add_u32_e32 v89, s28, v93
	v_cndmask_b32_e64 v88, v88, v95, s[42:43]
	v_add_u32_e32 v95, 64, v95
	ds_read_b128 v[100:103], v53
	ds_read_b128 v[104:107], v88 offset:16384
	v_mfma_f32_16x16x32_f16 v[6:9], v[62:65], v[66:69], v[6:9]
	ds_read_b128 v[108:111], v53 offset:1024
	v_mfma_f32_16x16x32_f16 v[26:29], v[54:57], v[70:73], v[26:29]
	ds_read_b128 v[112:115], v89 offset:16384
	v_mfma_f32_16x16x32_f16 v[30:33], v[80:83], v[58:61], v[30:33]
	ds_read_b128 v[116:119], v88 offset:18432
	v_mfma_f32_16x16x32_f16 v[22:25], v[80:83], v[66:69], v[22:25]
	ds_read_b128 v[120:123], v89 offset:18432
	v_mfma_f32_16x16x32_f16 v[18:21], v[54:57], v[74:77], v[18:21]
	ds_read_b128 v[124:127], v53 offset:8192
	v_mfma_f32_16x16x32_f16 v[14:17], v[84:87], v[58:61], v[14:17]
	ds_read_b128 v[128:131], v53 offset:9216
	v_mfma_f32_16x16x32_f16 v[10:13], v[62:65], v[70:73], v[10:13]
	v_mfma_f32_16x16x32_f16 v[6:9], v[84:87], v[66:69], v[6:9]
	v_mfma_f32_16x16x32_f16 v[2:5], v[62:65], v[74:77], v[2:5]
	s_add_i32 s36, s36, 1
	s_add_u32 s26, s26, 64
	s_add_i32 s28, s37, 1
	s_cmp_lg_u32 s37, 4
	s_cselect_b32 s37, s28, 0
	s_add_i32 s28, s38, 1
	s_cmp_lg_u32 s38, 4
	s_cselect_b32 s38, s28, 0
	s_waitcnt lgkmcnt(0)
	v_mfma_f32_16x16x32_f16 v[14:17], v[108:111], v[104:107], v[14:17]
	v_mfma_f32_16x16x32_f16 v[30:33], v[100:103], v[104:107], v[30:33]
	v_mfma_f32_16x16x32_f16 v[22:25], v[100:103], v[112:115], v[22:25]
	v_mfma_f32_16x16x32_f16 v[6:9], v[108:111], v[112:115], v[6:9]
	v_mfma_f32_16x16x32_f16 v[26:29], v[100:103], v[116:119], v[26:29]
	v_mfma_f32_16x16x32_f16 v[30:33], v[124:127], v[104:107], v[30:33]
	v_mfma_f32_16x16x32_f16 v[22:25], v[124:127], v[112:115], v[22:25]
	v_mfma_f32_16x16x32_f16 v[18:21], v[100:103], v[120:123], v[18:21]
	v_mfma_f32_16x16x32_f16 v[14:17], v[128:131], v[104:107], v[14:17]
	v_mfma_f32_16x16x32_f16 v[10:13], v[108:111], v[116:119], v[10:13]
	v_mfma_f32_16x16x32_f16 v[6:9], v[128:131], v[112:115], v[6:9]
	v_mfma_f32_16x16x32_f16 v[2:5], v[108:111], v[120:123], v[2:5]
	s_nop 1

.LBB1_36:
	s_waitcnt lgkmcnt(0)
	s_setprio 1
	v_mfma_f32_16x16x32_f16 v[62:65], v[88:91], v[104:107], v[62:65]
	v_mfma_f32_16x16x32_f16 v[58:61], v[88:91], v[108:111], v[58:61]
	v_mfma_f32_16x16x32_f16 v[54:57], v[88:91], v[112:115], v[54:57]
	v_mfma_f32_16x16x32_f16 v[50:53], v[88:91], v[116:119], v[50:53]
	v_mfma_f32_16x16x32_f16 v[46:49], v[92:95], v[104:107], v[46:49]
	v_mfma_f32_16x16x32_f16 v[42:45], v[92:95], v[108:111], v[42:45]
	v_mfma_f32_16x16x32_f16 v[38:41], v[92:95], v[112:115], v[38:41]
	v_mfma_f32_16x16x32_f16 v[34:37], v[92:95], v[116:119], v[34:37]
	s_waitcnt vmcnt(6)
	s_barrier
	s_mul_i32 s49, s46, 0xc000
	s_add_u32 s50, s49, s3
	s_add_u32 s51, s49, s2
	v_add3_u32 v120, s50, v86, v85
	v_add3_u32 v121, s50, v86, v84
	v_add3_u32 v122, s51, v81, v85
	v_add3_u32 v123, s51, v81, v84
	s_mul_i32 s49, s45, 0xc000
	s_add_u32 s49, s49, s44
	ds_read_b128 v[176:179], v120
	ds_read_b128 v[180:183], v120 offset:2048
	ds_read_b128 v[184:187], v120 offset:4096
	ds_read_b128 v[188:191], v120 offset:6144
	v_mfma_f32_16x16x32_f16 v[30:33], v[96:99], v[104:107], v[30:33]
	ds_read_b128 v[192:195], v122
	v_mfma_f32_16x16x32_f16 v[26:29], v[96:99], v[108:111], v[26:29]
	ds_read_b128 v[196:199], v122 offset:2048
	v_mfma_f32_16x16x32_f16 v[22:25], v[96:99], v[112:115], v[22:25]
	ds_read_b128 v[200:203], v122 offset:4096
	v_mfma_f32_16x16x32_f16 v[18:21], v[96:99], v[116:119], v[18:21]
	ds_read_b128 v[204:207], v122 offset:6144
	v_mfma_f32_16x16x32_f16 v[14:17], v[100:103], v[104:107], v[14:17]
	ds_read_b128 v[208:211], v121
	v_mfma_f32_16x16x32_f16 v[10:13], v[100:103], v[108:111], v[10:13]
	ds_read_b128 v[212:215], v121 offset:2048
	v_mfma_f32_16x16x32_f16 v[6:9], v[100:103], v[112:115], v[6:9]
	ds_read_b128 v[216:219], v121 offset:4096
	v_mfma_f32_16x16x32_f16 v[2:5], v[100:103], v[116:119], v[2:5]
	ds_read_b128 v[220:223], v121 offset:6144
	v_mfma_f32_16x16x32_f16 v[62:65], v[144:147], v[160:163], v[62:65]
	ds_read_b128 v[224:227], v123
	v_mfma_f32_16x16x32_f16 v[58:61], v[144:147], v[164:167], v[58:61]
	ds_read_b128 v[228:231], v123 offset:2048
	v_mfma_f32_16x16x32_f16 v[54:57], v[144:147], v[168:171], v[54:57]
	ds_read_b128 v[232:235], v123 offset:4096
	v_mfma_f32_16x16x32_f16 v[50:53], v[144:147], v[172:175], v[50:53]
	ds_read_b128 v[236:239], v123 offset:6144
	v_mfma_f32_16x16x32_f16 v[46:49], v[148:151], v[160:163], v[46:49]
	v_mfma_f32_16x16x32_f16 v[42:45], v[148:151], v[164:167], v[42:45]
	s_mov_b32 m0, s49
	v_lshl_add_u64 v[124:125], v[76:77], 0, s[0:1]
	global_load_lds_dwordx4 v[124:125], off
	v_mfma_f32_16x16x32_f16 v[38:41], v[148:151], v[168:171], v[38:41]
	v_mfma_f32_16x16x32_f16 v[34:37], v[148:151], v[172:175], v[34:37]
	s_add_u32 m0, s49, 0x2000
	v_lshl_add_u64 v[124:125], v[74:75], 0, s[0:1]
	global_load_lds_dwordx4 v[124:125], off
	v_mfma_f32_16x16x32_f16 v[30:33], v[152:155], v[160:163], v[30:33]
	v_mfma_f32_16x16x32_f16 v[26:29], v[152:155], v[164:167], v[26:29]
	s_add_u32 m0, s49, 0x4000
	v_lshl_add_u64 v[124:125], v[70:71], 0, s[0:1]
	global_load_lds_dwordx4 v[124:125], off
	v_mfma_f32_16x16x32_f16 v[22:25], v[152:155], v[168:171], v[22:25]
	v_mfma_f32_16x16x32_f16 v[18:21], v[152:155], v[172:175], v[18:21]
	s_add_u32 m0, s49, 0x6000
	v_lshl_add_u64 v[124:125], v[68:69], 0, s[0:1]
	global_load_lds_dwordx4 v[124:125], off
	v_mfma_f32_16x16x32_f16 v[14:17], v[156:159], v[160:163], v[14:17]
	v_mfma_f32_16x16x32_f16 v[10:13], v[156:159], v[164:167], v[10:13]
	s_add_u32 m0, s49, 0x8000
	v_lshl_add_u64 v[124:125], v[72:73], 0, s[0:1]
	global_load_lds_dwordx4 v[124:125], off
	v_mfma_f32_16x16x32_f16 v[6:9], v[156:159], v[168:171], v[6:9]
	v_mfma_f32_16x16x32_f16 v[2:5], v[156:159], v[172:175], v[2:5]
	s_add_u32 m0, s49, 0xa000
	v_lshl_add_u64 v[124:125], v[66:67], 0, s[0:1]
	global_load_lds_dwordx4 v[124:125], off
	s_setprio 0
	s_add_u32 s0, s0, 0x80
	s_addc_u32 s1, s1, 0
	s_add_i32 s48, s48, 1
	s_add_i32 s49, s45, 1
	s_cmp_lg_u32 s45, 2
	s_cselect_b32 s45, s49, 0
	s_add_i32 s49, s46, 1
	s_cmp_lg_u32 s46, 2
	s_cselect_b32 s46, s49, 0
	s_waitcnt lgkmcnt(0)
	s_setprio 1
	v_mfma_f32_16x16x32_f16 v[62:65], v[176:179], v[192:195], v[62:65]
	v_mfma_f32_16x16x32_f16 v[58:61], v[176:179], v[196:199], v[58:61]
	v_mfma_f32_16x16x32_f16 v[54:57], v[176:179], v[200:203], v[54:57]
	v_mfma_f32_16x16x32_f16 v[50:53], v[176:179], v[204:207], v[50:53]
	v_mfma_f32_16x16x32_f16 v[46:49], v[180:183], v[192:195], v[46:49]
	v_mfma_f32_16x16x32_f16 v[42:45], v[180:183], v[196:199], v[42:45]
	v_mfma_f32_16x16x32_f16 v[38:41], v[180:183], v[200:203], v[38:41]
	v_mfma_f32_16x16x32_f16 v[34:37], v[180:183], v[204:207], v[34:37]
	s_waitcnt vmcnt(6)
	s_barrier
	s_mul_i32 s49, s46, 0xc000
	s_add_u32 s50, s49, s3
	s_add_u32 s51, s49, s2
	v_add3_u32 v120, s50, v86, v85
	v_add3_u32 v121, s50, v86, v84
	v_add3_u32 v122, s51, v81, v85
	v_add3_u32 v123, s51, v81, v84
	s_mul_i32 s49, s45, 0xc000
	s_add_u32 s49, s49, s44
	ds_read_b128 v[88:91], v120
	ds_read_b128 v[92:95], v120 offset:2048
	ds_read_b128 v[96:99], v120 offset:4096
	ds_read_b128 v[100:103], v120 offset:6144
	v_mfma_f32_16x16x32_f16 v[30:33], v[184:187], v[192:195], v[30:33]
	ds_read_b128 v[104:107], v122
	v_mfma_f32_16x16x32_f16 v[26:29], v[184:187], v[196:199], v[26:29]
	ds_read_b128 v[108:111], v122 offset:2048
	v_mfma_f32_16x16x32_f16 v[22:25], v[184:187], v[200:203], v[22:25]
	ds_read_b128 v[112:115], v122 offset:4096
	v_mfma_f32_16x16x32_f16 v[18:21], v[184:187], v[204:207], v[18:21]
	ds_read_b128 v[116:119], v122 offset:6144
	v_mfma_f32_16x16x32_f16 v[14:17], v[188:191], v[192:195], v[14:17]
	ds_read_b128 v[144:147], v121
	v_mfma_f32_16x16x32_f16 v[10:13], v[188:191], v[196:199], v[10:13]
	ds_read_b128 v[148:151], v121 offset:2048
	v_mfma_f32_16x16x32_f16 v[6:9], v[188:191], v[200:203], v[6:9]
	ds_read_b128 v[152:155], v121 offset:4096
	v_mfma_f32_16x16x32_f16 v[2:5], v[188:191], v[204:207], v[2:5]
	ds_read_b128 v[156:159], v121 offset:6144
	v_mfma_f32_16x16x32_f16 v[62:65], v[208:211], v[224:227], v[62:65]
	ds_read_b128 v[160:163], v123
	v_mfma_f32_16x16x32_f16 v[58:61], v[208:211], v[228:231], v[58:61]
	ds_read_b128 v[164:167], v123 offset:2048
	v_mfma_f32_16x16x32_f16 v[54:57], v[208:211], v[232:235], v[54:57]
	ds_read_b128 v[168:171], v123 offset:4096
	v_mfma_f32_16x16x32_f16 v[50:53], v[208:211], v[236:239], v[50:53]
	ds_read_b128 v[172:175], v123 offset:6144
	v_mfma_f32_16x16x32_f16 v[46:49], v[212:215], v[224:227], v[46:49]
	v_mfma_f32_16x16x32_f16 v[42:45], v[212:215], v[228:231], v[42:45]
	s_mov_b32 m0, s49
	v_lshl_add_u64 v[124:125], v[76:77], 0, s[0:1]
	global_load_lds_dwordx4 v[124:125], off
	v_mfma_f32_16x16x32_f16 v[38:41], v[212:215], v[232:235], v[38:41]
	v_mfma_f32_16x16x32_f16 v[34:37], v[212:215], v[236:239], v[34:37]
	s_add_u32 m0, s49, 0x2000
	v_lshl_add_u64 v[124:125], v[74:75], 0, s[0:1]
	global_load_lds_dwordx4 v[124:125], off
	v_mfma_f32_16x16x32_f16 v[30:33], v[216:219], v[224:227], v[30:33]
	v_mfma_f32_16x16x32_f16 v[26:29], v[216:219], v[228:231], v[26:29]
	s_add_u32 m0, s49, 0x4000
	v_lshl_add_u64 v[124:125], v[70:71], 0, s[0:1]
	global_load_lds_dwordx4 v[124:125], off
	v_mfma_f32_16x16x32_f16 v[22:25], v[216:219], v[232:235], v[22:25]
	v_mfma_f32_16x16x32_f16 v[18:21], v[216:219], v[236:239], v[18:21]
	s_add_u32 m0, s49, 0x6000
	v_lshl_add_u64 v[124:125], v[68:69], 0, s[0:1]
	global_load_lds_dwordx4 v[124:125], off
	v_mfma_f32_16x16x32_f16 v[14:17], v[220:223], v[224:227], v[14:17]
	v_mfma_f32_16x16x32_f16 v[10:13], v[220:223], v[228:231], v[10:13]
	s_add_u32 m0, s49, 0x8000
	v_lshl_add_u64 v[124:125], v[72:73], 0, s[0:1]
	global_load_lds_dwordx4 v[124:125], off
	v_mfma_f32_16x16x32_f16 v[6:9], v[220:223], v[232:235], v[6:9]
	v_mfma_f32_16x16x32_f16 v[2:5], v[220:223], v[236:239], v[2:5]
	s_add_u32 m0, s49, 0xa000
	v_lshl_add_u64 v[124:125], v[66:67], 0, s[0:1]
	global_load_lds_dwordx4 v[124:125], off
	s_setprio 0
	s_add_u32 s0, s0, 0x80
	s_addc_u32 s1, s1, 0
	s_add_i32 s48, s48, 1
	s_add_i32 s49, s45, 1
	s_cmp_lg_u32 s45, 2
	s_cselect_b32 s45, s49, 0
	s_add_i32 s49, s46, 1
	s_cmp_lg_u32 s46, 2
	s_cselect_b32 s46, s49, 0
	s_cmp_lt_u32 s48, 12
	s_cbranch_scc1 .LBB1_36
	s_waitcnt lgkmcnt(0)
	s_setprio 1
	v_mfma_f32_16x16x32_f16 v[62:65], v[88:91], v[104:107], v[62:65]
	v_mfma_f32_16x16x32_f16 v[58:61], v[88:91], v[108:111], v[58:61]
	v_mfma_f32_16x16x32_f16 v[54:57], v[88:91], v[112:115], v[54:57]
	v_mfma_f32_16x16x32_f16 v[50:53], v[88:91], v[116:119], v[50:53]
	v_mfma_f32_16x16x32_f16 v[46:49], v[92:95], v[104:107], v[46:49]
	v_mfma_f32_16x16x32_f16 v[42:45], v[92:95], v[108:111], v[42:45]
	v_mfma_f32_16x16x32_f16 v[38:41], v[92:95], v[112:115], v[38:41]
	v_mfma_f32_16x16x32_f16 v[34:37], v[92:95], v[116:119], v[34:37]
	s_waitcnt vmcnt(6)
	s_barrier
	s_mul_i32 s49, s46, 0xc000
	s_add_u32 s50, s49, s3
	s_add_u32 s51, s49, s2
	v_add3_u32 v120, s50, v86, v85
	v_add3_u32 v121, s50, v86, v84
	v_add3_u32 v122, s51, v81, v85
	v_add3_u32 v123, s51, v81, v84
	s_mul_i32 s49, s45, 0xc000
	s_add_u32 s49, s49, s44
	ds_read_b128 v[176:179], v120
	ds_read_b128 v[180:183], v120 offset:2048
	ds_read_b128 v[184:187], v120 offset:4096
	ds_read_b128 v[188:191], v120 offset:6144
	v_mfma_f32_16x16x32_f16 v[30:33], v[96:99], v[104:107], v[30:33]
	ds_read_b128 v[192:195], v122
	v_mfma_f32_16x16x32_f16 v[26:29], v[96:99], v[108:111], v[26:29]
	ds_read_b128 v[196:199], v122 offset:2048
	v_mfma_f32_16x16x32_f16 v[22:25], v[96:99], v[112:115], v[22:25]
	ds_read_b128 v[200:203], v122 offset:4096
	v_mfma_f32_16x16x32_f16 v[18:21], v[96:99], v[116:119], v[18:21]
	ds_read_b128 v[204:207], v122 offset:6144
	v_mfma_f32_16x16x32_f16 v[14:17], v[100:103], v[104:107], v[14:17]
	ds_read_b128 v[208:211], v121
	v_mfma_f32_16x16x32_f16 v[10:13], v[100:103], v[108:111], v[10:13]
	ds_read_b128 v[212:215], v121 offset:2048
	v_mfma_f32_16x16x32_f16 v[6:9], v[100:103], v[112:115], v[6:9]
	ds_read_b128 v[216:219], v121 offset:4096
	v_mfma_f32_16x16x32_f16 v[2:5], v[100:103], v[116:119], v[2:5]
	ds_read_b128 v[220:223], v121 offset:6144
	v_mfma_f32_16x16x32_f16 v[62:65], v[144:147], v[160:163], v[62:65]
	ds_read_b128 v[224:227], v123
	v_mfma_f32_16x16x32_f16 v[58:61], v[144:147], v[164:167], v[58:61]
	ds_read_b128 v[228:231], v123 offset:2048
	v_mfma_f32_16x16x32_f16 v[54:57], v[144:147], v[168:171], v[54:57]
	ds_read_b128 v[232:235], v123 offset:4096
	v_mfma_f32_16x16x32_f16 v[50:53], v[144:147], v[172:175], v[50:53]
	ds_read_b128 v[236:239], v123 offset:6144
	v_mfma_f32_16x16x32_f16 v[46:49], v[148:151], v[160:163], v[46:49]
	v_mfma_f32_16x16x32_f16 v[42:45], v[148:151], v[164:167], v[42:45]
	s_mov_b32 m0, s49
	v_lshl_add_u64 v[124:125], v[76:77], 0, s[0:1]
	global_load_lds_dwordx4 v[124:125], off
	v_mfma_f32_16x16x32_f16 v[38:41], v[148:151], v[168:171], v[38:41]
	v_mfma_f32_16x16x32_f16 v[34:37], v[148:151], v[172:175], v[34:37]
	s_add_u32 m0, s49, 0x2000
	v_lshl_add_u64 v[124:125], v[74:75], 0, s[0:1]
	global_load_lds_dwordx4 v[124:125], off
	v_mfma_f32_16x16x32_f16 v[30:33], v[152:155], v[160:163], v[30:33]
	v_mfma_f32_16x16x32_f16 v[26:29], v[152:155], v[164:167], v[26:29]
	s_add_u32 m0, s49, 0x4000
	v_lshl_add_u64 v[124:125], v[70:71], 0, s[0:1]
	global_load_lds_dwordx4 v[124:125], off
	v_mfma_f32_16x16x32_f16 v[22:25], v[152:155], v[168:171], v[22:25]
	v_mfma_f32_16x16x32_f16 v[18:21], v[152:155], v[172:175], v[18:21]
	s_add_u32 m0, s49, 0x6000
	v_lshl_add_u64 v[124:125], v[68:69], 0, s[0:1]
	global_load_lds_dwordx4 v[124:125], off
	v_mfma_f32_16x16x32_f16 v[14:17], v[156:159], v[160:163], v[14:17]
	v_mfma_f32_16x16x32_f16 v[10:13], v[156:159], v[164:167], v[10:13]
	s_add_u32 m0, s49, 0x8000
	v_lshl_add_u64 v[124:125], v[72:73], 0, s[0:1]
	global_load_lds_dwordx4 v[124:125], off
	v_mfma_f32_16x16x32_f16 v[6:9], v[156:159], v[168:171], v[6:9]
	v_mfma_f32_16x16x32_f16 v[2:5], v[156:159], v[172:175], v[2:5]
	s_add_u32 m0, s49, 0xa000
	v_lshl_add_u64 v[124:125], v[66:67], 0, s[0:1]
	global_load_lds_dwordx4 v[124:125], off
	s_setprio 0
	s_add_u32 s0, s0, 0x80
	s_addc_u32 s1, s1, 0
	s_add_i32 s48, s48, 1
	s_add_i32 s49, s45, 1
	s_cmp_lg_u32 s45, 2
	s_cselect_b32 s45, s49, 0
	s_add_i32 s49, s46, 1
	s_cmp_lg_u32 s46, 2
	s_cselect_b32 s46, s49, 0
	s_waitcnt lgkmcnt(0)
	s_setprio 1
	v_mfma_f32_16x16x32_f16 v[62:65], v[176:179], v[192:195], v[62:65]
	v_mfma_f32_16x16x32_f16 v[58:61], v[176:179], v[196:199], v[58:61]
	v_mfma_f32_16x16x32_f16 v[54:57], v[176:179], v[200:203], v[54:57]
	v_mfma_f32_16x16x32_f16 v[50:53], v[176:179], v[204:207], v[50:53]
	v_mfma_f32_16x16x32_f16 v[46:49], v[180:183], v[192:195], v[46:49]
	v_mfma_f32_16x16x32_f16 v[42:45], v[180:183], v[196:199], v[42:45]
	v_mfma_f32_16x16x32_f16 v[38:41], v[180:183], v[200:203], v[38:41]
	v_mfma_f32_16x16x32_f16 v[34:37], v[180:183], v[204:207], v[34:37]
	s_waitcnt vmcnt(6)
	s_barrier
	s_mul_i32 s49, s46, 0xc000
	s_add_u32 s50, s49, s3
	s_add_u32 s51, s49, s2
	v_add3_u32 v120, s50, v86, v85
	v_add3_u32 v121, s50, v86, v84
	v_add3_u32 v122, s51, v81, v85
	v_add3_u32 v123, s51, v81, v84
	ds_read_b128 v[88:91], v120
	ds_read_b128 v[92:95], v120 offset:2048
	ds_read_b128 v[96:99], v120 offset:4096
	ds_read_b128 v[100:103], v120 offset:6144
	v_mfma_f32_16x16x32_f16 v[30:33], v[184:187], v[192:195], v[30:33]
	ds_read_b128 v[104:107], v122
	v_mfma_f32_16x16x32_f16 v[26:29], v[184:187], v[196:199], v[26:29]
	ds_read_b128 v[108:111], v122 offset:2048
	v_mfma_f32_16x16x32_f16 v[22:25], v[184:187], v[200:203], v[22:25]
	ds_read_b128 v[112:115], v122 offset:4096
	v_mfma_f32_16x16x32_f16 v[18:21], v[184:187], v[204:207], v[18:21]
	ds_read_b128 v[116:119], v122 offset:6144
	v_mfma_f32_16x16x32_f16 v[14:17], v[188:191], v[192:195], v[14:17]
	ds_read_b128 v[144:147], v121
	v_mfma_f32_16x16x32_f16 v[10:13], v[188:191], v[196:199], v[10:13]
	ds_read_b128 v[148:151], v121 offset:2048
	v_mfma_f32_16x16x32_f16 v[6:9], v[188:191], v[200:203], v[6:9]
	ds_read_b128 v[152:155], v121 offset:4096
	v_mfma_f32_16x16x32_f16 v[2:5], v[188:191], v[204:207], v[2:5]
	ds_read_b128 v[156:159], v121 offset:6144
	v_mfma_f32_16x16x32_f16 v[62:65], v[208:211], v[224:227], v[62:65]
	ds_read_b128 v[160:163], v123
	v_mfma_f32_16x16x32_f16 v[58:61], v[208:211], v[228:231], v[58:61]
	ds_read_b128 v[164:167], v123 offset:2048
	v_mfma_f32_16x16x32_f16 v[54:57], v[208:211], v[232:235], v[54:57]
	ds_read_b128 v[168:171], v123 offset:4096
	v_mfma_f32_16x16x32_f16 v[50:53], v[208:211], v[236:239], v[50:53]
	ds_read_b128 v[172:175], v123 offset:6144
	v_mfma_f32_16x16x32_f16 v[46:49], v[212:215], v[224:227], v[46:49]
	v_mfma_f32_16x16x32_f16 v[42:45], v[212:215], v[228:231], v[42:45]
	v_mfma_f32_16x16x32_f16 v[38:41], v[212:215], v[232:235], v[38:41]
	v_mfma_f32_16x16x32_f16 v[34:37], v[212:215], v[236:239], v[34:37]
	v_mfma_f32_16x16x32_f16 v[30:33], v[216:219], v[224:227], v[30:33]
	v_mfma_f32_16x16x32_f16 v[26:29], v[216:219], v[228:231], v[26:29]
	v_mfma_f32_16x16x32_f16 v[22:25], v[216:219], v[232:235], v[22:25]
	v_mfma_f32_16x16x32_f16 v[18:21], v[216:219], v[236:239], v[18:21]
	v_mfma_f32_16x16x32_f16 v[14:17], v[220:223], v[224:227], v[14:17]
	v_mfma_f32_16x16x32_f16 v[10:13], v[220:223], v[228:231], v[10:13]
	v_mfma_f32_16x16x32_f16 v[6:9], v[220:223], v[232:235], v[6:9]
	v_mfma_f32_16x16x32_f16 v[2:5], v[220:223], v[236:239], v[2:5]
	s_setprio 0
	s_add_u32 s0, s0, 0x80
	s_addc_u32 s1, s1, 0
	s_add_i32 s48, s48, 1
	s_add_i32 s49, s45, 1
	s_cmp_lg_u32 s45, 2
	s_cselect_b32 s45, s49, 0
	s_add_i32 s49, s46, 1
	s_cmp_lg_u32 s46, 2
	s_cselect_b32 s46, s49, 0
	s_waitcnt lgkmcnt(0)
	s_setprio 1
	v_mfma_f32_16x16x32_f16 v[62:65], v[88:91], v[104:107], v[62:65]
	v_mfma_f32_16x16x32_f16 v[58:61], v[88:91], v[108:111], v[58:61]
	v_mfma_f32_16x16x32_f16 v[54:57], v[88:91], v[112:115], v[54:57]
	v_mfma_f32_16x16x32_f16 v[50:53], v[88:91], v[116:119], v[50:53]
	v_mfma_f32_16x16x32_f16 v[46:49], v[92:95], v[104:107], v[46:49]
	v_mfma_f32_16x16x32_f16 v[42:45], v[92:95], v[108:111], v[42:45]
	v_mfma_f32_16x16x32_f16 v[38:41], v[92:95], v[112:115], v[38:41]
	v_mfma_f32_16x16x32_f16 v[34:37], v[92:95], v[116:119], v[34:37]
	s_waitcnt vmcnt(0)
	s_barrier
	s_mul_i32 s49, s46, 0xc000
	s_add_u32 s50, s49, s3
	s_add_u32 s51, s49, s2
	v_add3_u32 v120, s50, v86, v85
	v_add3_u32 v121, s50, v86, v84
	v_add3_u32 v122, s51, v81, v85
	v_add3_u32 v123, s51, v81, v84
	ds_read_b128 v[176:179], v120
	ds_read_b128 v[180:183], v120 offset:2048
	ds_read_b128 v[184:187], v120 offset:4096
	ds_read_b128 v[188:191], v120 offset:6144
	v_mfma_f32_16x16x32_f16 v[30:33], v[96:99], v[104:107], v[30:33]
	ds_read_b128 v[192:195], v122
	v_mfma_f32_16x16x32_f16 v[26:29], v[96:99], v[108:111], v[26:29]
	ds_read_b128 v[196:199], v122 offset:2048
	v_mfma_f32_16x16x32_f16 v[22:25], v[96:99], v[112:115], v[22:25]
	ds_read_b128 v[200:203], v122 offset:4096
	v_mfma_f32_16x16x32_f16 v[18:21], v[96:99], v[116:119], v[18:21]
	ds_read_b128 v[204:207], v122 offset:6144
	v_mfma_f32_16x16x32_f16 v[14:17], v[100:103], v[104:107], v[14:17]
	ds_read_b128 v[208:211], v121
	v_mfma_f32_16x16x32_f16 v[10:13], v[100:103], v[108:111], v[10:13]
	ds_read_b128 v[212:215], v121 offset:2048
	v_mfma_f32_16x16x32_f16 v[6:9], v[100:103], v[112:115], v[6:9]
	ds_read_b128 v[216:219], v121 offset:4096
	v_mfma_f32_16x16x32_f16 v[2:5], v[100:103], v[116:119], v[2:5]
	ds_read_b128 v[220:223], v121 offset:6144
	v_mfma_f32_16x16x32_f16 v[62:65], v[144:147], v[160:163], v[62:65]
	ds_read_b128 v[224:227], v123
	v_mfma_f32_16x16x32_f16 v[58:61], v[144:147], v[164:167], v[58:61]
	ds_read_b128 v[228:231], v123 offset:2048
	v_mfma_f32_16x16x32_f16 v[54:57], v[144:147], v[168:171], v[54:57]
	ds_read_b128 v[232:235], v123 offset:4096
	v_mfma_f32_16x16x32_f16 v[50:53], v[144:147], v[172:175], v[50:53]
	ds_read_b128 v[236:239], v123 offset:6144
	v_mfma_f32_16x16x32_f16 v[46:49], v[148:151], v[160:163], v[46:49]
	v_mfma_f32_16x16x32_f16 v[42:45], v[148:151], v[164:167], v[42:45]
	v_mfma_f32_16x16x32_f16 v[38:41], v[148:151], v[168:171], v[38:41]
	v_mfma_f32_16x16x32_f16 v[34:37], v[148:151], v[172:175], v[34:37]
	v_mfma_f32_16x16x32_f16 v[30:33], v[152:155], v[160:163], v[30:33]
	v_mfma_f32_16x16x32_f16 v[26:29], v[152:155], v[164:167], v[26:29]
	v_mfma_f32_16x16x32_f16 v[22:25], v[152:155], v[168:171], v[22:25]
	v_mfma_f32_16x16x32_f16 v[18:21], v[152:155], v[172:175], v[18:21]
	v_mfma_f32_16x16x32_f16 v[14:17], v[156:159], v[160:163], v[14:17]
	v_mfma_f32_16x16x32_f16 v[10:13], v[156:159], v[164:167], v[10:13]
	v_mfma_f32_16x16x32_f16 v[6:9], v[156:159], v[168:171], v[6:9]
	v_mfma_f32_16x16x32_f16 v[2:5], v[156:159], v[172:175], v[2:5]
	s_setprio 0
	s_add_u32 s0, s0, 0x80
	s_addc_u32 s1, s1, 0
	s_add_i32 s48, s48, 1
	s_add_i32 s49, s45, 1
	s_cmp_lg_u32 s45, 2
	s_cselect_b32 s45, s49, 0
	s_add_i32 s49, s46, 1
	s_cmp_lg_u32 s46, 2
	s_cselect_b32 s46, s49, 0
	s_waitcnt lgkmcnt(0)
	s_setprio 1
	v_mfma_f32_16x16x32_f16 v[62:65], v[176:179], v[192:195], v[62:65]
	v_mfma_f32_16x16x32_f16 v[58:61], v[176:179], v[196:199], v[58:61]
	v_mfma_f32_16x16x32_f16 v[54:57], v[176:179], v[200:203], v[54:57]
	v_mfma_f32_16x16x32_f16 v[50:53], v[176:179], v[204:207], v[50:53]
	v_mfma_f32_16x16x32_f16 v[46:49], v[180:183], v[192:195], v[46:49]
	v_mfma_f32_16x16x32_f16 v[42:45], v[180:183], v[196:199], v[42:45]
	v_mfma_f32_16x16x32_f16 v[38:41], v[180:183], v[200:203], v[38:41]
	v_mfma_f32_16x16x32_f16 v[34:37], v[180:183], v[204:207], v[34:37]
	v_mfma_f32_16x16x32_f16 v[30:33], v[184:187], v[192:195], v[30:33]
	v_mfma_f32_16x16x32_f16 v[26:29], v[184:187], v[196:199], v[26:29]
	v_mfma_f32_16x16x32_f16 v[22:25], v[184:187], v[200:203], v[22:25]
	v_mfma_f32_16x16x32_f16 v[18:21], v[184:187], v[204:207], v[18:21]
	v_mfma_f32_16x16x32_f16 v[14:17], v[188:191], v[192:195], v[14:17]
	v_mfma_f32_16x16x32_f16 v[10:13], v[188:191], v[196:199], v[10:13]
	v_mfma_f32_16x16x32_f16 v[6:9], v[188:191], v[200:203], v[6:9]
	v_mfma_f32_16x16x32_f16 v[2:5], v[188:191], v[204:207], v[2:5]
	v_mfma_f32_16x16x32_f16 v[62:65], v[208:211], v[224:227], v[62:65]
	v_mfma_f32_16x16x32_f16 v[58:61], v[208:211], v[228:231], v[58:61]
	v_mfma_f32_16x16x32_f16 v[54:57], v[208:211], v[232:235], v[54:57]
	v_mfma_f32_16x16x32_f16 v[50:53], v[208:211], v[236:239], v[50:53]
	v_mfma_f32_16x16x32_f16 v[46:49], v[212:215], v[224:227], v[46:49]
	v_mfma_f32_16x16x32_f16 v[42:45], v[212:215], v[228:231], v[42:45]
	v_mfma_f32_16x16x32_f16 v[38:41], v[212:215], v[232:235], v[38:41]
	v_mfma_f32_16x16x32_f16 v[34:37], v[212:215], v[236:239], v[34:37]
	v_mfma_f32_16x16x32_f16 v[30:33], v[216:219], v[224:227], v[30:33]
	v_mfma_f32_16x16x32_f16 v[26:29], v[216:219], v[228:231], v[26:29]
	v_mfma_f32_16x16x32_f16 v[22:25], v[216:219], v[232:235], v[22:25]
	v_mfma_f32_16x16x32_f16 v[18:21], v[216:219], v[236:239], v[18:21]
	v_mfma_f32_16x16x32_f16 v[14:17], v[220:223], v[224:227], v[14:17]
	v_mfma_f32_16x16x32_f16 v[10:13], v[220:223], v[228:231], v[10:13]
	v_mfma_f32_16x16x32_f16 v[6:9], v[220:223], v[232:235], v[6:9]
	v_mfma_f32_16x16x32_f16 v[2:5], v[220:223], v[236:239], v[2:5]
	s_setprio 0
	s_branch .Lqk_epi_start
